# speedup vs baseline: 1.0591x; 1.0363x over previous
.LBB3_46:
	s_or_b64 exec, exec, s[0:1]
	v_add_u32_e32 v97, v125, v137
	ds_read_b128 v[0:3], v97
	v_add_u32_e32 v96, v125, v138
	ds_read_b128 v[4:7], v96
	v_mad_u64_u32 v[8:9], s[0:1], v145, s33, v[112:113]
	s_waitcnt lgkmcnt(1)
	global_store_dwordx4 v[8:9], v[0:3], off sc1
	s_nop 1
	v_mad_u64_u32 v[0:1], s[0:1], v146, s33, v[112:113]
	s_waitcnt lgkmcnt(0)
	global_store_dwordx4 v[0:1], v[4:7], off sc1
	s_and_saveexec_b64 s[0:1], s[60:61]
	s_cbranch_execz .LBB3_39
	ds_read_b128 v[0:3], v125 offset:2304
	v_add3_u32 v4, v124, s72, 16
	v_mad_u64_u32 v[4:5], s[66:67], v4, s33, v[112:113]
	s_waitcnt lgkmcnt(0)
	global_store_dwordx4 v[4:5], v[0:3], off sc1
	s_branch .LBB3_39

.LBB3_52:
	s_or_b64 exec, exec, s[0:1]
	v_mov_b32_e32 v0, 0xffffffbc
	v_lshl_add_u32 v2, v126, 2, v114
	v_mov_b32_e32 v1, -1
	v_mad_u64_u32 v[0:1], s[0:1], v2, 17, v[0:1]
	ds_read_b128 v[2:5], v97
	ds_read_b128 v[6:9], v96
	v_add_u32_e32 v1, v115, v0
	s_movk_i32 s0, 0x480
	v_mad_u64_u32 v[10:11], s[2:3], v1, s0, v[112:113]
	v_add_u32_e32 v1, v116, v0
	s_waitcnt lgkmcnt(1)
	global_store_dwordx4 v[10:11], v[2:5], off sc1
	s_nop 1
	v_mad_u64_u32 v[2:3], s[2:3], v1, s0, v[112:113]
	s_waitcnt lgkmcnt(0)
	global_store_dwordx4 v[2:3], v[6:9], off sc1
	s_and_saveexec_b64 s[2:3], s[60:61]
	s_cbranch_execz .LBB3_54
	ds_read_b128 v[2:5], v125 offset:2304
	v_add_u32_e32 v0, 16, v0
	v_mad_u64_u32 v[0:1], s[0:1], v0, s0, v[112:113]
	s_waitcnt lgkmcnt(0)
	global_store_dwordx4 v[0:1], v[2:5], off sc1

.LBB4_15:
	v_and_b32_e32 v66, 0xc0, v0
	v_or_b32_e32 v75, s20, v66
	v_or_b32_e32 v66, v75, v1
	v_ashrrev_i32_e32 v67, 31, v66
	s_waitcnt lgkmcnt(0)
	v_lshl_add_u64 v[66:67], v[66:67], 2, s[8:9]
	s_waitcnt vmcnt(0)
	s_barrier
	global_load_dword v70, v[66:67], off
	s_nop 0
	global_load_dword v67, v[66:67], off offset:128
	s_load_dword s4, s[0:1], 0x48
	v_lshlrev_b32_e32 v66, 7, v0
	v_lshlrev_b32_e32 v71, 2, v0
	v_bfe_u32 v68, v0, 4, 2
	v_add_u32_e32 v69, s15, v72
	v_lshlrev_b32_e32 v0, 5, v0
	v_and_b32_e32 v66, 0xe000, v66
	v_and_b32_e32 v76, 60, v71
	v_and_b32_e32 v72, 0x400, v0
	v_or_b32_e32 v74, v68, v69
	v_lshl_or_b32 v73, v1, 2, v66
	v_or_b32_e32 v0, v75, v76
	v_lshlrev_b32_e32 v71, 8, v68
	v_lshl_or_b32 v66, v76, 2, v66
	v_ashrrev_i32_e32 v1, 31, v0
	v_or_b32_e32 v75, v73, v72
	v_cmp_gt_i32_e32 vcc, s7, v74
	v_add_u32_e32 v76, 0x800, v75
	v_add_u32_e32 v77, 0x1000, v75
	v_add_u32_e32 v78, 0x1800, v75
	s_waitcnt vmcnt(1)
	v_add_f32_e32 v50, v50, v70
	s_waitcnt vmcnt(0)
	v_add_f32_e32 v34, v34, v67
	v_add_f32_e32 v51, v51, v70
	v_add_f32_e32 v52, v52, v70
	v_add_f32_e32 v53, v53, v70
	v_add_f32_e32 v54, v54, v70
	v_add_f32_e32 v55, v55, v70
	v_add_f32_e32 v56, v56, v70
	v_add_f32_e32 v57, v57, v70
	v_add_f32_e32 v58, v58, v70
	v_add_f32_e32 v59, v59, v70
	v_add_f32_e32 v60, v60, v70
	v_add_f32_e32 v61, v61, v70
	v_add_f32_e32 v62, v62, v70
	v_add_f32_e32 v63, v63, v70
	v_add_f32_e32 v64, v64, v70
	v_add_f32_e32 v65, v65, v70
	v_add_f32_e32 v35, v35, v67
	v_add_f32_e32 v36, v36, v67
	v_add_f32_e32 v37, v37, v67
	v_add_f32_e32 v38, v38, v67
	v_add_f32_e32 v39, v39, v67
	v_add_f32_e32 v40, v40, v67
	v_add_f32_e32 v41, v41, v67
	v_add_f32_e32 v42, v42, v67
	v_add_f32_e32 v43, v43, v67
	v_add_f32_e32 v44, v44, v67
	v_add_f32_e32 v45, v45, v67
	v_add_f32_e32 v46, v46, v67
	v_add_f32_e32 v47, v47, v67
	v_add_f32_e32 v48, v48, v67
	v_add_f32_e32 v49, v49, v67
	ds_write2_b32 v75, v50, v34 offset1:32
	ds_write2_b32 v75, v51, v35 offset0:64 offset1:96
	ds_write2_b32 v75, v52, v36 offset0:128 offset1:160
	ds_write2_b32 v75, v53, v37 offset0:192 offset1:224
	ds_write2_b32 v76, v54, v38 offset1:32
	ds_write2_b32 v76, v55, v39 offset0:64 offset1:96
	ds_write2_b32 v76, v56, v40 offset0:128 offset1:160
	ds_write2_b32 v76, v57, v41 offset0:192 offset1:224
	ds_write2_b32 v77, v58, v42 offset1:32
	ds_write2_b32 v77, v59, v43 offset0:64 offset1:96
	ds_write2_b32 v77, v60, v44 offset0:128 offset1:160
	ds_write2_b32 v77, v61, v45 offset0:192 offset1:224
	ds_write2_b32 v78, v62, v46 offset1:32
	ds_write2_b32 v78, v63, v47 offset0:64 offset1:96
	ds_write2_b32 v78, v64, v48 offset0:128 offset1:160
	ds_write2_b32 v78, v65, v49 offset0:192 offset1:224
	s_and_saveexec_b64 s[0:1], vcc
	s_cbranch_execz .LBB4_17
	v_add_u32_e32 v34, v66, v71
	ds_read_b128 v[34:37], v34
	s_waitcnt lgkmcnt(0)
	v_mad_i64_i32 v[38:39], s[8:9], v74, s4, v[0:1]
	v_lshl_add_u64 v[40:41], v[38:39], 2, s[10:11]
	global_store_dwordx4 v[40:41], v[34:37], off sc1 nt
	s_nop 1
	v_cvt_pk_f16_f32 v37, v36, v37
	v_cvt_pk_f16_f32 v36, v34, v35
	v_lshl_add_u64 v[34:35], v[38:39], 1, s[2:3]
	global_store_dwordx2 v[34:35], v[36:37], off
.LBB4_17:
	s_or_b64 exec, exec, s[0:1]
	v_or_b32_e32 v38, 4, v68
	v_or_b32_e32 v35, v38, v69
	v_lshlrev_b32_e32 v34, 8, v38
	v_cmp_gt_i32_e32 vcc, s7, v35
	s_and_saveexec_b64 s[0:1], vcc
	s_cbranch_execz .LBB4_19
	v_add_u32_e32 v36, v66, v34
	ds_read_b128 v[40:43], v36
	s_waitcnt lgkmcnt(0)
	v_mad_i64_i32 v[36:37], s[8:9], v35, s4, v[0:1]
	v_lshl_add_u64 v[44:45], v[36:37], 2, s[10:11]
	v_lshl_add_u64 v[36:37], v[36:37], 1, s[2:3]
	global_store_dwordx4 v[44:45], v[40:43], off sc1 nt
	s_nop 1
	v_cvt_pk_f16_f32 v43, v42, v43
	v_cvt_pk_f16_f32 v42, v40, v41
	global_store_dwordx2 v[36:37], v[42:43], off
.LBB4_19:
	s_or_b64 exec, exec, s[0:1]
	v_or_b32_e32 v40, 8, v68
	v_or_b32_e32 v36, v40, v69
	v_lshlrev_b32_e32 v35, 8, v40
	v_cmp_gt_i32_e32 vcc, s7, v36
	s_and_saveexec_b64 s[0:1], vcc
	s_cbranch_execz .LBB4_21
	v_add_u32_e32 v37, v66, v35
	ds_read_b128 v[42:45], v37
	s_waitcnt lgkmcnt(0)
	v_mad_i64_i32 v[36:37], s[8:9], v36, s4, v[0:1]
	v_lshl_add_u64 v[46:47], v[36:37], 2, s[10:11]
	v_lshl_add_u64 v[36:37], v[36:37], 1, s[2:3]
	global_store_dwordx4 v[46:47], v[42:45], off sc1 nt
	s_nop 1
	v_cvt_pk_f16_f32 v45, v44, v45
	v_cvt_pk_f16_f32 v44, v42, v43
	global_store_dwordx2 v[36:37], v[44:45], off
.LBB4_21:
	s_or_b64 exec, exec, s[0:1]
	v_or_b32_e32 v42, 12, v68
	v_or_b32_e32 v37, v42, v69
	v_lshlrev_b32_e32 v36, 8, v42
	v_cmp_gt_i32_e32 vcc, s7, v37
	s_and_saveexec_b64 s[0:1], vcc
	s_cbranch_execz .LBB4_23
	v_add_u32_e32 v39, v66, v36
	ds_read_b128 v[44:47], v39
	s_waitcnt lgkmcnt(0)
	v_mad_i64_i32 v[48:49], s[8:9], v37, s4, v[0:1]
	v_lshl_add_u64 v[50:51], v[48:49], 2, s[10:11]
	global_store_dwordx4 v[50:51], v[44:47], off sc1 nt
	s_nop 1
	v_cvt_pk_f16_f32 v47, v46, v47
	v_cvt_pk_f16_f32 v46, v44, v45
	v_lshl_add_u64 v[44:45], v[48:49], 1, s[2:3]
	global_store_dwordx2 v[44:45], v[46:47], off
.LBB4_23:
	s_or_b64 exec, exec, s[0:1]
	v_or_b32_e32 v44, 16, v68
	v_or_b32_e32 v39, v44, v69
	v_lshlrev_b32_e32 v37, 8, v44
	v_cmp_gt_i32_e32 vcc, s7, v39
	s_and_saveexec_b64 s[0:1], vcc
	s_cbranch_execz .LBB4_25
	v_add_u32_e32 v41, v66, v37
	ds_read_b128 v[46:49], v41
	s_waitcnt lgkmcnt(0)
	v_mad_i64_i32 v[50:51], s[8:9], v39, s4, v[0:1]
	v_lshl_add_u64 v[52:53], v[50:51], 2, s[10:11]
	global_store_dwordx4 v[52:53], v[46:49], off sc1 nt
	s_nop 1
	v_cvt_pk_f16_f32 v49, v48, v49
	v_cvt_pk_f16_f32 v48, v46, v47
	v_lshl_add_u64 v[46:47], v[50:51], 1, s[2:3]
	global_store_dwordx2 v[46:47], v[48:49], off
.LBB4_25:
	s_or_b64 exec, exec, s[0:1]
	v_or_b32_e32 v45, 20, v68
	v_or_b32_e32 v41, v45, v69
	v_lshlrev_b32_e32 v39, 8, v45
	v_cmp_gt_i32_e32 vcc, s7, v41
	s_and_saveexec_b64 s[0:1], vcc
	s_cbranch_execz .LBB4_27
	v_add_u32_e32 v43, v66, v39
	ds_read_b128 v[46:49], v43
	s_waitcnt lgkmcnt(0)
	v_mad_i64_i32 v[50:51], s[8:9], v41, s4, v[0:1]
	v_lshl_add_u64 v[52:53], v[50:51], 2, s[10:11]
	global_store_dwordx4 v[52:53], v[46:49], off sc1 nt
	s_nop 1
	v_cvt_pk_f16_f32 v49, v48, v49
	v_cvt_pk_f16_f32 v48, v46, v47
	v_lshl_add_u64 v[46:47], v[50:51], 1, s[2:3]
	global_store_dwordx2 v[46:47], v[48:49], off
.LBB4_27:
	s_or_b64 exec, exec, s[0:1]
	v_or_b32_e32 v46, 24, v68
	v_or_b32_e32 v43, v46, v69
	v_lshlrev_b32_e32 v41, 8, v46
	v_cmp_gt_i32_e32 vcc, s7, v43
	s_and_saveexec_b64 s[0:1], vcc
	s_cbranch_execz .LBB4_29
	v_add_u32_e32 v47, v66, v41
	ds_read_b128 v[48:51], v47
	s_waitcnt lgkmcnt(0)
	v_mad_i64_i32 v[52:53], s[8:9], v43, s4, v[0:1]
	v_lshl_add_u64 v[54:55], v[52:53], 2, s[10:11]
	global_store_dwordx4 v[54:55], v[48:51], off sc1 nt
	s_nop 1
	v_cvt_pk_f16_f32 v51, v50, v51
	v_cvt_pk_f16_f32 v50, v48, v49
	v_lshl_add_u64 v[48:49], v[52:53], 1, s[2:3]
	global_store_dwordx2 v[48:49], v[50:51], off
.LBB4_29:
	s_or_b64 exec, exec, s[0:1]
	v_or_b32_e32 v47, 28, v68
	v_or_b32_e32 v48, v47, v69
	v_lshlrev_b32_e32 v43, 8, v47
	v_cmp_gt_i32_e32 vcc, s7, v48
	s_and_saveexec_b64 s[0:1], vcc
	s_cbranch_execz .LBB4_31
	v_add_u32_e32 v49, v66, v43
	ds_read_b128 v[50:53], v49
	s_waitcnt lgkmcnt(0)
	v_mad_i64_i32 v[48:49], s[8:9], v48, s4, v[0:1]
	v_lshl_add_u64 v[54:55], v[48:49], 2, s[10:11]
	v_lshl_add_u64 v[48:49], v[48:49], 1, s[2:3]
	global_store_dwordx4 v[54:55], v[50:53], off sc1 nt
	s_nop 1
	v_cvt_pk_f16_f32 v53, v52, v53
	v_cvt_pk_f16_f32 v52, v50, v51
	global_store_dwordx2 v[48:49], v[52:53], off
.LBB4_31:
	s_or_b64 exec, exec, s[0:1]
	v_add_f32_e32 v18, v18, v70
	v_add_u32_e32 v48, v73, v72
	v_add_f32_e32 v2, v2, v67
	v_add_f32_e32 v19, v19, v70
	ds_write2_b32 v48, v18, v2 offset1:32
	v_add_f32_e32 v2, v3, v67
	v_add_f32_e32 v20, v20, v70
	ds_write2_b32 v48, v19, v2 offset0:64 offset1:96
	v_add_f32_e32 v2, v4, v67
	v_add_f32_e32 v21, v21, v70
	ds_write2_b32 v48, v20, v2 offset0:128 offset1:160
	v_add_f32_e32 v2, v5, v67
	v_add_f32_e32 v22, v22, v70
	ds_write2_b32 v48, v21, v2 offset0:192 offset1:224
	v_add_f32_e32 v2, v6, v67
	v_add_u32_e32 v3, 0x800, v48
	v_add_f32_e32 v23, v23, v70
	ds_write2_b32 v3, v22, v2 offset1:32
	v_add_f32_e32 v2, v7, v67
	v_add_f32_e32 v24, v24, v70
	ds_write2_b32 v3, v23, v2 offset0:64 offset1:96
	v_add_f32_e32 v2, v8, v67
	v_add_f32_e32 v25, v25, v70
	ds_write2_b32 v3, v24, v2 offset0:128 offset1:160
	v_add_f32_e32 v2, v9, v67
	v_add_f32_e32 v26, v26, v70
	ds_write2_b32 v3, v25, v2 offset0:192 offset1:224
	v_add_f32_e32 v2, v10, v67
	v_add_u32_e32 v3, 0x1000, v48
	v_add_f32_e32 v27, v27, v70
	ds_write2_b32 v3, v26, v2 offset1:32
	v_add_f32_e32 v2, v11, v67
	v_add_f32_e32 v28, v28, v70
	ds_write2_b32 v3, v27, v2 offset0:64 offset1:96
	v_add_f32_e32 v2, v12, v67
	v_add_f32_e32 v29, v29, v70
	ds_write2_b32 v3, v28, v2 offset0:128 offset1:160
	v_add_f32_e32 v2, v13, v67
	v_add_f32_e32 v30, v30, v70
	ds_write2_b32 v3, v29, v2 offset0:192 offset1:224
	v_add_f32_e32 v2, v14, v67
	v_add_u32_e32 v3, 0x1800, v48
	v_add_f32_e32 v31, v31, v70
	ds_write2_b32 v3, v30, v2 offset1:32
	v_add_f32_e32 v2, v15, v67
	v_add_f32_e32 v32, v32, v70
	ds_write2_b32 v3, v31, v2 offset0:64 offset1:96
	v_add_f32_e32 v2, v16, v67
	v_add_f32_e32 v33, v33, v70
	ds_write2_b32 v3, v32, v2 offset0:128 offset1:160
	v_add_f32_e32 v2, v17, v67
	ds_write2_b32 v3, v33, v2 offset0:192 offset1:224
	v_or_b32_e32 v2, 32, v69
	v_or_b32_e32 v3, v68, v2
	v_cmp_gt_i32_e32 vcc, s7, v3
	s_and_saveexec_b64 s[0:1], vcc
	s_cbranch_execz .LBB4_33
	v_add_u32_e32 v4, v66, v71
	ds_read_b128 v[4:7], v4
	s_waitcnt lgkmcnt(0)
	v_mad_i64_i32 v[8:9], s[8:9], v3, s4, v[0:1]
	v_lshl_add_u64 v[10:11], v[8:9], 2, s[10:11]
	global_store_dwordx4 v[10:11], v[4:7], off sc1 nt
	s_nop 1
	v_cvt_pk_f16_f32 v7, v6, v7
	v_cvt_pk_f16_f32 v6, v4, v5
	v_lshl_add_u64 v[4:5], v[8:9], 1, s[2:3]
	global_store_dwordx2 v[4:5], v[6:7], off
.LBB4_33:
	s_or_b64 exec, exec, s[0:1]
	v_or_b32_e32 v3, v38, v2
	v_cmp_gt_i32_e32 vcc, s7, v3
	s_and_saveexec_b64 s[0:1], vcc
	s_cbranch_execz .LBB4_35
	v_add_u32_e32 v4, v66, v34
	ds_read_b128 v[4:7], v4
	s_waitcnt lgkmcnt(0)
	v_mad_i64_i32 v[8:9], s[8:9], v3, s4, v[0:1]
	v_lshl_add_u64 v[10:11], v[8:9], 2, s[10:11]
	global_store_dwordx4 v[10:11], v[4:7], off sc1 nt
	s_nop 1
	v_cvt_pk_f16_f32 v7, v6, v7
	v_cvt_pk_f16_f32 v6, v4, v5
	v_lshl_add_u64 v[4:5], v[8:9], 1, s[2:3]
	global_store_dwordx2 v[4:5], v[6:7], off
.LBB4_35:
	s_or_b64 exec, exec, s[0:1]
	v_or_b32_e32 v3, v40, v2
	v_cmp_gt_i32_e32 vcc, s7, v3
	s_and_saveexec_b64 s[0:1], vcc
	s_cbranch_execz .LBB4_37
	v_add_u32_e32 v4, v66, v35
	ds_read_b128 v[4:7], v4
	s_waitcnt lgkmcnt(0)
	v_mad_i64_i32 v[8:9], s[8:9], v3, s4, v[0:1]
	v_lshl_add_u64 v[10:11], v[8:9], 2, s[10:11]
	global_store_dwordx4 v[10:11], v[4:7], off sc1 nt
	s_nop 1
	v_cvt_pk_f16_f32 v7, v6, v7
	v_cvt_pk_f16_f32 v6, v4, v5
	v_lshl_add_u64 v[4:5], v[8:9], 1, s[2:3]
	global_store_dwordx2 v[4:5], v[6:7], off
.LBB4_37:
	s_or_b64 exec, exec, s[0:1]
	v_or_b32_e32 v3, v42, v2
	v_cmp_gt_i32_e32 vcc, s7, v3
	s_and_saveexec_b64 s[0:1], vcc
	s_cbranch_execz .LBB4_39
	v_add_u32_e32 v4, v66, v36
	ds_read_b128 v[4:7], v4
	s_waitcnt lgkmcnt(0)
	v_mad_i64_i32 v[8:9], s[8:9], v3, s4, v[0:1]
	v_lshl_add_u64 v[10:11], v[8:9], 2, s[10:11]
	global_store_dwordx4 v[10:11], v[4:7], off sc1 nt
	s_nop 1
	v_cvt_pk_f16_f32 v7, v6, v7
	v_cvt_pk_f16_f32 v6, v4, v5
	v_lshl_add_u64 v[4:5], v[8:9], 1, s[2:3]
	global_store_dwordx2 v[4:5], v[6:7], off
.LBB4_39:
	s_or_b64 exec, exec, s[0:1]
	v_or_b32_e32 v3, v44, v2
	v_cmp_gt_i32_e32 vcc, s7, v3
	s_and_saveexec_b64 s[0:1], vcc
	s_cbranch_execz .LBB4_41
	v_add_u32_e32 v4, v66, v37
	ds_read_b128 v[4:7], v4
	s_waitcnt lgkmcnt(0)
	v_mad_i64_i32 v[8:9], s[8:9], v3, s4, v[0:1]
	v_lshl_add_u64 v[10:11], v[8:9], 2, s[10:11]
	global_store_dwordx4 v[10:11], v[4:7], off sc1 nt
	s_nop 1
	v_cvt_pk_f16_f32 v7, v6, v7
	v_cvt_pk_f16_f32 v6, v4, v5
	v_lshl_add_u64 v[4:5], v[8:9], 1, s[2:3]
	global_store_dwordx2 v[4:5], v[6:7], off
.LBB4_41:
	s_or_b64 exec, exec, s[0:1]
	v_or_b32_e32 v3, v45, v2
	v_cmp_gt_i32_e32 vcc, s7, v3
	s_and_saveexec_b64 s[0:1], vcc
	s_cbranch_execz .LBB4_43
	v_add_u32_e32 v4, v66, v39
	ds_read_b128 v[4:7], v4
	s_waitcnt lgkmcnt(0)
	v_mad_i64_i32 v[8:9], s[8:9], v3, s4, v[0:1]
	v_lshl_add_u64 v[10:11], v[8:9], 2, s[10:11]
	global_store_dwordx4 v[10:11], v[4:7], off sc1 nt
	s_nop 1
	v_cvt_pk_f16_f32 v7, v6, v7
	v_cvt_pk_f16_f32 v6, v4, v5
	v_lshl_add_u64 v[4:5], v[8:9], 1, s[2:3]
	global_store_dwordx2 v[4:5], v[6:7], off
.LBB4_43:
	s_or_b64 exec, exec, s[0:1]
	v_or_b32_e32 v3, v46, v2
	v_cmp_gt_i32_e32 vcc, s7, v3
	s_and_saveexec_b64 s[0:1], vcc
	s_cbranch_execz .LBB4_45
	v_add_u32_e32 v4, v66, v41
	ds_read_b128 v[4:7], v4
	s_waitcnt lgkmcnt(0)
	v_mad_i64_i32 v[8:9], s[8:9], v3, s4, v[0:1]
	v_lshl_add_u64 v[10:11], v[8:9], 2, s[10:11]
	global_store_dwordx4 v[10:11], v[4:7], off sc1 nt
	s_nop 1
	v_cvt_pk_f16_f32 v7, v6, v7
	v_cvt_pk_f16_f32 v6, v4, v5
	v_lshl_add_u64 v[4:5], v[8:9], 1, s[2:3]
	global_store_dwordx2 v[4:5], v[6:7], off
.LBB4_45:
	s_or_b64 exec, exec, s[0:1]
	v_or_b32_e32 v2, v47, v2
	v_cmp_gt_i32_e32 vcc, s7, v2
	s_and_saveexec_b64 s[0:1], vcc
	s_cbranch_execz .LBB4_47
	v_add_u32_e32 v3, v66, v43
	ds_read_b128 v[4:7], v3
	s_waitcnt lgkmcnt(0)
	v_mad_i64_i32 v[0:1], s[0:1], v2, s4, v[0:1]
	v_lshl_add_u64 v[2:3], v[0:1], 2, s[10:11]
	v_lshl_add_u64 v[0:1], v[0:1], 1, s[2:3]
	global_store_dwordx4 v[2:3], v[4:7], off sc1 nt
	v_cvt_pk_f16_f32 v3, v6, v7
	v_cvt_pk_f16_f32 v2, v4, v5
	global_store_dwordx2 v[0:1], v[2:3], off
